# A/B of the static raise: s_setprio 1 for waves 0-3 instead of 4-7 (flips deleted)
# baseline (speedup 1.0000x reference)
; template <class Epi, class Sched, class Prob>
; __device__ __forceinline__ void gemm_phase(LAS unsigned char* lds, LAS unsigned char* lds_epi, const Prob g, const Sched& S, const Epi& E, int wid) {
;     ...
;     for (;;) {
;         const bool has_next = S.next(ui + 1, nxt);
;         const char* nA = has_next ? g.a_base(nxt) : cA; const char* nB = has_next ? g.b_base(nxt) : cB;
; _Pragma("clang loop unroll(disable)")
;         for (int t = 0; t < nt; t += 2) {
;             const bool last = (t == nt - 2);
;             const char* a1 = cA + (size_t)(t + 1) * kstep;
;             const char* a2 = last ? nA : cA + (size_t)(t + 2) * kstep; const char* b2 = last ? nB : cB + (size_t)(t + 2) * kstep;
.LBB0_261:
	s_ashr_i32 s3, s2, 31
	s_lshl_b64 s[48:49], s[2:3], 20
	s_add_u32 s48, s33, s48
	s_addc_u32 s49, s39, s49
	s_and_b64 s[50:51], s[46:47], exec
	s_cselect_b32 s3, s49, s15
	s_cselect_b32 s77, s48, s14
	s_ashr_i32 s45, s44, 31
	s_lshl_b64 s[50:51], s[44:45], 20
	s_add_u32 s50, s56, s50
	s_addc_u32 s51, s57, s51
	s_and_b64 s[54:55], s[46:47], exec
	s_cselect_b32 s45, s51, s53
	s_cselect_b32 s78, s50, s52
	s_add_u32 s14, s14, 0x80
	s_addc_u32 s15, s15, 0
	s_add_u32 s79, s52, 0x100
	v_mov_b32_e32 v44, 0
	s_addc_u32 s80, s53, 0
	s_mov_b32 s81, -2
	s_cmp_ge_u32 s91, 0x100
	s_cbranch_scc1 .Lyoung_0
	s_setprio 1

; template <class Epi, class Sched, class Prob>
; __device__ __forceinline__ void gemm_phase(LAS unsigned char* lds, LAS unsigned char* lds_epi, const Prob g, const Sched& S, const Epi& E, int wid) {
;     ...
;     for (;;) {
;         const bool has_next = S.next(ui + 1, nxt);
;         const char* nA = has_next ? g.a_base(nxt) : cA; const char* nB = has_next ? g.b_base(nxt) : cB;
; _Pragma("clang loop unroll(disable)")
;         for (int t = 0; t < nt; t += 2) {
;             const bool last = (t == nt - 2);
;             const char* a1 = cA + (size_t)(t + 1) * kstep;
;             const char* a2 = last ? nA : cA + (size_t)(t + 2) * kstep; const char* b2 = last ? nB : cB + (size_t)(t + 2) * kstep;
.LBB0_1155:
	s_ashr_i32 s25, s24, 31
	s_lshl_b64 s[28:29], s[24:25], 20
	s_add_u32 s28, s44, s28
	s_addc_u32 s29, s45, s29
	s_and_b64 s[30:31], s[34:35], exec
	s_cselect_b32 s25, s29, s39
	s_cselect_b32 s27, s28, s38
	s_ashr_i32 s23, s22, 31
	s_lshl_b64 s[30:31], s[22:23], 20
	s_add_u32 s30, s46, s30
	s_addc_u32 s31, s47, s31
	s_and_b64 s[42:43], s[34:35], exec
	s_cselect_b32 s23, s31, s41
	s_cselect_b32 s37, s30, s40
	s_add_u32 s38, s38, 0x80
	s_addc_u32 s39, s39, 0
	s_add_u32 s66, s40, 0x100
	s_addc_u32 s67, s41, 0
	s_mov_b32 s68, -2
	s_cmp_ge_u32 s91, 0x100
	s_cbranch_scc1 .Lyoung_1
	s_setprio 1

; template <class Epi, class Sched, class Prob>
; __device__ __forceinline__ void gemm_phase(LAS unsigned char* lds, LAS unsigned char* lds_epi, const Prob g, const Sched& S, const Epi& E, int wid) {
;     ...
;     for (;;) {
;         const bool has_next = S.next(ui + 1, nxt);
;         const char* nA = has_next ? g.a_base(nxt) : cA; const char* nB = has_next ? g.b_base(nxt) : cB;
; _Pragma("clang loop unroll(disable)")
;         for (int t = 0; t < nt; t += 2) {
;             const bool last = (t == nt - 2);
;             const char* a1 = cA + (size_t)(t + 1) * kstep;
;             const char* a2 = last ? nA : cA + (size_t)(t + 2) * kstep; const char* b2 = last ? nB : cB + (size_t)(t + 2) * kstep;
.LBB0_1247:
	s_ashr_i32 s3, s2, 31
	s_lshl_b64 s[24:25], s[2:3], 19
	s_add_u32 s24, s36, s24
	s_addc_u32 s25, s37, s25
	s_and_b64 s[26:27], s[22:23], exec
	s_cselect_b32 s3, s25, s11
	s_cselect_b32 s54, s24, s10
	s_ashr_i32 s21, s20, 31
	s_lshl_b64 s[26:27], s[20:21], 19
	s_add_u32 s26, s40, s26
	s_addc_u32 s27, s41, s27
	s_and_b64 s[34:35], s[22:23], exec
	s_cselect_b32 s21, s27, s31
	s_cselect_b32 s55, s26, s30
	s_add_u32 s10, s10, 0x80
	s_addc_u32 s11, s11, 0
	s_add_u32 s56, s30, 0x100
	v_mov_b32_e32 v32, 0
	s_addc_u32 s58, s31, 0
	s_mov_b32 s59, -2
	s_cmp_ge_u32 s91, 0x100
	s_cbranch_scc1 .Lyoung_2
	s_setprio 1

; template <class Epi, class Sched, class Prob>
; __device__ __forceinline__ void gemm_phase(LAS unsigned char* lds, LAS unsigned char* lds_epi, const Prob g, const Sched& S, const Epi& E, int wid) {
;     ...
;     for (;;) {
;         const bool has_next = S.next(ui + 1, nxt);
;         const char* nA = has_next ? g.a_base(nxt) : cA; const char* nB = has_next ? g.b_base(nxt) : cB;
; _Pragma("clang loop unroll(disable)")
;         for (int t = 0; t < nt; t += 2) {
;             const bool last = (t == nt - 2);
;             const char* a1 = cA + (size_t)(t + 1) * kstep;
;             const char* a2 = last ? nA : cA + (size_t)(t + 2) * kstep; const char* b2 = last ? nB : cB + (size_t)(t + 2) * kstep;
.LBB0_1335:
	s_add_u32 s28, s28, 0x80
	s_addc_u32 s29, s29, 0
	s_add_u32 s60, s30, 0x100
	s_addc_u32 s61, s31, 0
	s_mov_b32 s62, -2
	s_cmp_ge_u32 s91, 0x100
	s_cbranch_scc1 .Lyoung_3
	s_setprio 1

; template <class Epi, class Sched, class Prob>
; __device__ __forceinline__ void gemm_phase(LAS unsigned char* lds, LAS unsigned char* lds_epi, const Prob g, const Sched& S, const Epi& E, int wid) {
;     ...
;     for (;;) {
;         const bool has_next = S.next(ui + 1, nxt);
;         const char* nA = has_next ? g.a_base(nxt) : cA; const char* nB = has_next ? g.b_base(nxt) : cB;
; _Pragma("clang loop unroll(disable)")
;         for (int t = 0; t < nt; t += 2) {
;             const bool last = (t == nt - 2);
;             const char* a1 = cA + (size_t)(t + 1) * kstep;
;             const char* a2 = last ? nA : cA + (size_t)(t + 2) * kstep; const char* b2 = last ? nB : cB + (size_t)(t + 2) * kstep;
.LBB0_1433:
	s_ashr_i32 s17, s16, 31
	s_lshl_b64 s[40:41], s[16:17], 20
	s_add_u32 s40, s58, s40
	s_addc_u32 s41, s59, s41
	s_and_b64 s[42:43], s[36:37], exec
	s_cselect_b32 s17, s41, s11
	s_cselect_b32 s52, s40, s10
	s_ashr_i32 s35, s34, 31
	s_lshl_b64 s[42:43], s[34:35], 20
	s_add_u32 s42, s60, s42
	s_addc_u32 s43, s61, s43
	s_and_b64 s[48:49], s[36:37], exec
	s_cselect_b32 s35, s43, s47
	s_cselect_b32 s53, s42, s46
	s_add_u32 s54, s46, 0x100
	v_mov_b32_e32 v0, 0
	s_addc_u32 s55, s47, 0
	s_mov_b32 s87, -2
	s_cmp_ge_u32 s91, 0x100
	s_cbranch_scc1 .Lyoung_4
	s_setprio 1

; template <class Epi, class Sched, class Prob>
; __device__ __forceinline__ void gemm_phase(LAS unsigned char* lds, LAS unsigned char* lds_epi, const Prob g, const Sched& S, const Epi& E, int wid) {
;     ...
;     for (;;) {
;         const bool has_next = S.next(ui + 1, nxt);
;         const char* nA = has_next ? g.a_base(nxt) : cA; const char* nB = has_next ? g.b_base(nxt) : cB;
; _Pragma("clang loop unroll(disable)")
;         for (int t = 0; t < nt; t += 2) {
;             const bool last = (t == nt - 2);
;             const char* a1 = cA + (size_t)(t + 1) * kstep;
;             const char* a2 = last ? nA : cA + (size_t)(t + 2) * kstep; const char* b2 = last ? nB : cB + (size_t)(t + 2) * kstep;
.LBB0_1594:
	s_ashr_i32 s65, s64, 31
	s_lshl_b64 s[14:15], s[64:65], 20
	s_add_u32 s17, s40, s14
	s_addc_u32 s19, s41, s15
	s_ashr_i32 s14, s62, 1
	s_ashr_i32 s15, s14, 31
	s_lshl_b64 s[14:15], s[14:15], 9
	s_add_u32 s68, s17, s14
	s_addc_u32 s69, s19, s15
	s_and_b64 s[14:15], s[66:67], exec
	s_cselect_b32 s17, s69, s9
	s_cselect_b32 s19, s68, s8
	s_ashr_i32 s63, s62, 31
	s_lshl_b64 s[14:15], s[62:63], 17
	s_add_u32 s70, s33, s14
	s_addc_u32 s71, s76, s15
	s_and_b64 s[14:15], s[66:67], exec
	v_mov_b32_e32 v0, 0
	s_cselect_b32 s26, s71, s11
	s_cselect_b32 s27, s70, s10
	s_mov_b64 s[20:21], -1
	s_mov_b64 s[14:15], 0
	s_cmp_ge_u32 s91, 0x100
	s_cbranch_scc1 .Lyoung_5
	s_setprio 1

; template <class Epi, class Sched, class Prob>
; __device__ __forceinline__ void gemm_phase(LAS unsigned char* lds, LAS unsigned char* lds_epi, const Prob g, const Sched& S, const Epi& E, int wid) {
;     ...
;     for (;;) {
;         const bool has_next = S.next(ui + 1, nxt);
;         const char* nA = has_next ? g.a_base(nxt) : cA; const char* nB = has_next ? g.b_base(nxt) : cB;
; _Pragma("clang loop unroll(disable)")
;         for (int t = 0; t < nt; t += 2) {
;             const bool last = (t == nt - 2);
;             const char* a1 = cA + (size_t)(t + 1) * kstep;
;             const char* a2 = last ? nA : cA + (size_t)(t + 2) * kstep; const char* b2 = last ? nB : cB + (size_t)(t + 2) * kstep;
.LBB0_1748:
	s_ashr_i32 s17, s16, 31
	s_lshl_b64 s[22:23], s[16:17], 20
	s_add_u32 s22, s33, s22
	s_addc_u32 s23, s36, s23
	s_and_b64 s[24:25], s[30:31], exec
	s_cselect_b32 s17, s23, s27
	s_cselect_b32 s19, s22, s26
	s_ashr_i32 s15, s14, 31
	s_lshl_b64 s[24:25], s[14:15], 20
	s_add_u32 s24, s37, s24
	s_addc_u32 s25, s40, s25
	s_and_b64 s[34:35], s[30:31], exec
	s_cselect_b32 s15, s25, s29
	s_cselect_b32 s54, s24, s28
	s_add_u32 s26, s26, 0x80
	s_addc_u32 s27, s27, 0
	s_add_u32 s55, s28, 0x100
	s_addc_u32 s56, s29, 0
	s_mov_b32 s57, -2
	s_cmp_ge_u32 s91, 0x100
	s_cbranch_scc1 .Lyoung_6
	s_setprio 1

; template <class Epi, class Sched, class Prob>
; __device__ __forceinline__ void gemm_phase(LAS unsigned char* lds, LAS unsigned char* lds_epi, const Prob g, const Sched& S, const Epi& E, int wid) {
;     ...
;     for (;;) {
;         const bool has_next = S.next(ui + 1, nxt);
;         const char* nA = has_next ? g.a_base(nxt) : cA; const char* nB = has_next ? g.b_base(nxt) : cB;
; _Pragma("clang loop unroll(disable)")
;         for (int t = 0; t < nt; t += 2) {
;             const bool last = (t == nt - 2);
;             const char* a1 = cA + (size_t)(t + 1) * kstep;
;             const char* a2 = last ? nA : cA + (size_t)(t + 2) * kstep; const char* b2 = last ? nB : cB + (size_t)(t + 2) * kstep;
.LBB0_2090:
	s_ashr_i32 s11, s10, 31
	s_lshl_b64 s[30:31], s[10:11], 19
	s_add_u32 s30, s51, s30
	s_addc_u32 s31, s52, s31
	s_and_b64 s[40:41], s[40:41], exec
	s_cselect_b32 s11, s31, s37
	s_cselect_b32 s29, s30, s36
	s_add_u32 s36, s36, 0x80
	v_mov_b32_e32 v32, 0
	s_addc_u32 s37, s37, 0
	v_lshl_add_u64 v[182:183], v[0:1], 0, s[22:23]
	s_mov_b32 s69, -2
	s_cmp_ge_u32 s91, 0x100
	s_cbranch_scc1 .Lyoung_7
	s_setprio 1

; template <class Epi, class Sched, class Prob>
; __device__ __forceinline__ void gemm_phase(LAS unsigned char* lds, LAS unsigned char* lds_epi, const Prob g, const Sched& S, const Epi& E, int wid) {
;     ...
;     for (;;) {
;         const bool has_next = S.next(ui + 1, nxt);
;         const char* nA = has_next ? g.a_base(nxt) : cA; const char* nB = has_next ? g.b_base(nxt) : cB;
; _Pragma("clang loop unroll(disable)")
;         for (int t = 0; t < nt; t += 2) {
;             const bool last = (t == nt - 2);
;             const char* a1 = cA + (size_t)(t + 1) * kstep;
;             const char* a2 = last ? nA : cA + (size_t)(t + 2) * kstep; const char* b2 = last ? nB : cB + (size_t)(t + 2) * kstep;
.LBB0_2172:
	s_add_u32 s36, s36, 0x80
	v_mov_b32_e32 v32, 0
	s_addc_u32 s37, s37, 0
	v_lshl_add_u64 v[186:187], v[0:1], 0, s[22:23]
	s_mov_b32 s64, -2
	s_cmp_ge_u32 s91, 0x100
	s_cbranch_scc1 .Lyoung_8
	s_setprio 1

; #define PG8_STAGE(bufoff, gbase, o0, o1) do { \
;         __builtin_amdgcn_global_load_lds((const unsigned*)((const char*)(gbase) + (o0)), (LAS unsigned*)(lds + (bufoff) + ldsw), 16, 0, 0); \
;         __builtin_amdgcn_global_load_lds((const unsigned*)((const char*)(gbase) + (o1)), (LAS unsigned*)(lds + (bufoff) + ldsw + 8192), 16, 0, 0); } while (0)
; #define PG8_WAIT_V(n) asm volatile("s_waitcnt vmcnt(" #n ")" ::: "memory")
; #define PG8_BAR __builtin_amdgcn_s_barrier()
; #define PG8_ACC_INIT(unit) do { if constexpr (Epi::ACC_INIT) { E.init(acc, unit, wr, wc, fr, fq); } else { \
;         _Pragma("unroll") for (int a = 0; a < 2; ++a) _Pragma("unroll") for (int b = 0; b < 2; ++b) _Pragma("unroll") for (int m = 0; m < 4; ++m) _Pragma("unroll") for (int n = 0; n < 2; ++n) acc[a][b][m][n] = (f32x4){0.f, 0.f, 0.f, 0.f}; } } while (0)
; template <class Epi, class Sched, class Prob>
; __device__ __forceinline__ void gemm_phase(LAS unsigned char* lds, LAS unsigned char* lds_epi, const Prob g, const Sched& S, const Epi& E, int wid) {
;     ...
;     const unsigned cA00 = (unsigned)Ra0 * lda2 + (unsigned)C0 * 2u, cA01 = (unsigned)Ra1 * lda2 + (unsigned)C1 * 2u, cA10 = cA00 + (unsigned)HALF * lda2, cA11 = cA01 + (unsigned)HALF * lda2;
;     f32x4 acc[2][2][4][2];
;     ...
;     PG8_ACC_INIT(cur);
;     bf16x8 At[4][2], B0[2][2], B1[2][2];
;     const char* cA = g.a_base(cur); const char* cB = g.b_base(cur);
;     PG8_STAGE(PG8_SB(0, 0), cB, vB0, vB1); PG8_STAGE(PG8_SB(0, 1), cB + hstepB, vB0, vB1); PG8_STAGE(PG8_SA(0, 0), cA, cA00, cA01); PG8_STAGE(PG8_SA(0, 1), cA, cA10, cA11);
;     if (wr == 1) PG8_BAR;
;     PG8_WAIT_V(2); PG8_BAR;
;     PG8_STAGE(PG8_SB(1, 0), cB + kstep, vB0, vB1); PG8_STAGE(PG8_SA(1, 0), cA + kstep, cA00, cA01); PG8_STAGE(PG8_SB(1, 1), cB + hstepB + kstep, vB0, vB1);
;     PG8_WAIT_V(6); PG8_BAR;
;     for (;;) {
.LBB0_2190:
	s_mov_b64 s[12:13], 0x80
	v_lshl_add_u64 v[6:7], v[6:7], 0, s[12:13]
	s_add_i32 m0, s25, 0x18000
	s_waitcnt vmcnt(2)
	s_barrier
	global_load_lds_dwordx4 v[6:7], off
	v_lshl_add_u64 v[2:3], v[2:3], 0, s[12:13]
	s_add_i32 m0, s25, 0x1a000
	s_add_i32 s29, s25, 0x8000
	s_add_i32 s30, s25, 0xa000
	global_load_lds_dwordx4 v[2:3], off
	v_lshl_add_u64 v[0:1], v[0:1], 0, s[12:13]
	s_mov_b32 m0, s29
	s_add_u32 s36, s10, 0xe0080
	global_load_lds_dwordx4 v[0:1], off
	v_lshl_add_u64 v[0:1], v[4:5], 0, s[12:13]
	s_mov_b32 m0, s30
	s_addc_u32 s37, s11, 0
	global_load_lds_dwordx4 v[0:1], off
	v_lshl_add_u64 v[0:1], s[36:37], 0, v[162:163]
	s_add_i32 m0, s25, 0x1c000
	s_mov_b32 s40, 0x1c000
	global_load_lds_dwordx4 v[0:1], off
	v_lshl_add_u64 v[0:1], s[36:37], 0, v[164:165]
	s_add_i32 m0, s25, 0x1e000
	s_add_u32 s36, s15, s21
	global_load_lds_dwordx4 v[0:1], off
	v_lshrrev_b32_e32 v1, 1, v200
	v_mul_lo_u32 v0, v203, s31
	s_addc_u32 s37, s14, 0
	v_mad_u64_u32 v[0:1], s[14:15], v1, s40, v[0:1]
	s_add_u32 s14, s8, s36
	s_addc_u32 s15, s9, s37
	s_add_i32 s17, s17, s18
	s_add_i32 s17, s17, s19
	v_and_b32_e32 v1, 1, v200
	s_add_i32 s17, s17, s20
	v_lshl_or_b32 v0, v1, 6, v0
	v_lshlrev_b32_e32 v1, 1, v206
	s_add_i32 s16, s17, s16
	v_add3_u32 v0, v0, v1, s35
	v_mov_b32_e32 v1, v163
	s_mul_hi_u32 s17, s16, 0xe00000
	s_mul_i32 s16, s16, 0xe00000
	v_lshl_add_u64 v[0:1], s[14:15], 0, v[0:1]
	s_mov_b64 s[36:37], 0x41000080
	s_add_u32 s16, s16, s34
	v_lshl_add_u64 v[174:175], v[0:1], 0, s[36:37]
	v_lshrrev_b32_e32 v1, 1, v199
	v_mul_lo_u32 v0, v201, s31
	s_addc_u32 s17, s17, s33
	v_mad_u64_u32 v[0:1], s[40:41], v1, s40, v[0:1]
	s_add_u32 s16, s16, s21
	v_and_b32_e32 v1, 1, v199
	s_addc_u32 s17, s17, 0
	v_lshl_or_b32 v0, v1, 6, v0
	v_lshlrev_b32_e32 v1, 1, v202
	s_add_u32 s16, s8, s16
	v_add3_u32 v0, v0, v1, s35
	v_mov_b32_e32 v1, v163
	s_addc_u32 s17, s9, s17
	v_lshl_add_u64 v[0:1], s[14:15], 0, v[0:1]
	s_add_u32 s31, s16, 0x27000100
	s_waitcnt vmcnt(6)
	v_lshl_add_u64 v[176:177], v[0:1], 0, s[36:37]
	s_addc_u32 s33, s17, 0
	s_add_i32 s37, 0, 0x10000
	s_add_i32 s41, 0, 0x14000
	s_add_i32 s43, 0, 0x18000
	s_add_i32 s45, 0, 0x1c000
	v_add_u32_e32 v161, s37, v204
	v_add_u32_e32 v186, s41, v204
	s_add_i32 s37, s37, s97
	s_add_i32 s41, s41, s97
	v_add_u32_e32 v188, s43, v204
	v_add_u32_e32 v189, s45, v204
	s_add_i32 s43, s43, s97
	s_add_i32 s45, s45, s97
	v_mov_b32_e32 v171, v163
	v_mov_b32_e32 v173, v163
	s_mov_b32 s34, -2
	s_mov_b64 s[16:17], 0
	v_add_u32_e32 v187, 0, v205
	s_add_i32 s35, s25, 0xc000
	s_add_i32 s36, s25, 0xe000
	s_add_i32 s40, s37, 0x2000
	s_add_i32 s42, s41, 0x2000
	s_add_i32 s44, s43, 0x2000
	s_add_i32 s46, s45, 0x2000
	v_mov_b64_e32 v[32:33], 0
	v_mov_b64_e32 v[34:35], 0
	v_mov_b64_e32 v[36:37], 0
	v_mov_b64_e32 v[38:39], 0
	v_mov_b64_e32 v[40:41], 0
	v_mov_b64_e32 v[42:43], 0
	v_mov_b64_e32 v[44:45], 0
	v_mov_b64_e32 v[46:47], 0
	v_mov_b64_e32 v[48:49], 0
	v_mov_b64_e32 v[50:51], 0
	v_mov_b64_e32 v[52:53], 0
	v_mov_b64_e32 v[54:55], 0
	v_mov_b64_e32 v[56:57], 0
	v_mov_b64_e32 v[58:59], 0
	v_mov_b64_e32 v[60:61], 0
	v_mov_b64_e32 v[62:63], 0
	v_mov_b64_e32 v[64:65], 0
	v_mov_b64_e32 v[66:67], 0
	v_mov_b64_e32 v[68:69], 0
	v_mov_b64_e32 v[70:71], 0
	v_mov_b64_e32 v[72:73], 0
	v_mov_b64_e32 v[74:75], 0
	v_mov_b64_e32 v[76:77], 0
	v_mov_b64_e32 v[78:79], 0
	v_mov_b64_e32 v[80:81], 0
	v_mov_b64_e32 v[82:83], 0
	v_mov_b64_e32 v[84:85], 0
	v_mov_b64_e32 v[86:87], 0
	v_mov_b64_e32 v[88:89], 0
	v_mov_b64_e32 v[90:91], 0
	v_mov_b64_e32 v[92:93], 0
	v_mov_b64_e32 v[94:95], 0
	v_mov_b64_e32 v[96:97], 0
	v_mov_b64_e32 v[98:99], 0
	v_mov_b64_e32 v[100:101], 0
	v_mov_b64_e32 v[102:103], 0
	v_mov_b64_e32 v[104:105], 0
	v_mov_b64_e32 v[106:107], 0
	v_mov_b64_e32 v[108:109], 0
	v_mov_b64_e32 v[110:111], 0
	v_mov_b64_e32 v[112:113], 0
	v_mov_b64_e32 v[114:115], 0
	v_mov_b64_e32 v[116:117], 0
	v_mov_b64_e32 v[118:119], 0
	v_mov_b64_e32 v[120:121], 0
	v_mov_b64_e32 v[122:123], 0
	v_mov_b64_e32 v[124:125], 0
	v_mov_b64_e32 v[126:127], 0
	v_mov_b64_e32 v[128:129], 0
	v_mov_b64_e32 v[130:131], 0
	v_mov_b64_e32 v[132:133], 0
	v_mov_b64_e32 v[134:135], 0
	v_mov_b64_e32 v[136:137], 0
	v_mov_b64_e32 v[138:139], 0
	v_mov_b64_e32 v[140:141], 0
	v_mov_b64_e32 v[142:143], 0
	v_mov_b64_e32 v[144:145], 0
	v_mov_b64_e32 v[146:147], 0
	v_mov_b64_e32 v[148:149], 0
	v_mov_b64_e32 v[150:151], 0
	v_mov_b64_e32 v[152:153], 0
	v_mov_b64_e32 v[154:155], 0
	v_mov_b64_e32 v[156:157], 0
	v_mov_b64_e32 v[158:159], 0
	s_barrier
	s_cmp_ge_u32 s91, 0x100
	s_cbranch_scc1 .Lyoung_9
	s_setprio 1
